# mLSTM S^T stage: counted LDS waits per tile so the first tiles' MFMAs overlap the remaining tiles' reads
# speedup vs baseline: 1.0028x; 1.0028x over previous
; #define LAS __attribute__((address_space(3)))
; __device__ __forceinline__ unsigned long long pack4bf(f32x4 v) { return (unsigned long long)pk2(v[0], v[1]) | ((unsigned long long)pk2(v[2], v[3]) << 32); }
; __device__ __forceinline__ void mlstm_scan_unit(Frame& F, int unit, LAS unsigned* bcnt, unsigned& btarget) {
;     ...
;         { const int tt = w; const int t = 16 * tt + fr; const float mxt = smx[t];
; #pragma unroll
;           for (int jt = 0; jt < 4; ++jt) { f32x4 acc = (f32x4){0.f, 0.f, 0.f, 0.f};
;               if (jt <= tt) {
; #pragma unroll
;                   for (int ks = 0; ks < 4; ++ks) { const s16x8 a = *(const LAS s16x8*)(Lk + (16 * jt + fr) * 136 + 32 * ks + 8 * fq), bq = *(const LAS s16x8*)(Lq + (16 * tt + fr) * 136 + 32 * ks + 8 * fq);
;                       acc = __builtin_amdgcn_mfma_f32_16x16x32_bf16(a, bq, acc, 0, 0, 0); }
;                   const f32x4 u4 = *(const LAS f32x4*)(su + 16 * jt + 4 * fq);
; #pragma unroll
;                   for (int rg_ = 0; rg_ < 4; ++rg_) { const int j = 16 * jt + 4 * fq + rg_; acc[rg_] = (j <= t) ? acc[rg_] * __expf(u4[rg_] - mxt) : 0.f; } }
;               *(LAS unsigned long long*)(Ls + t * 72 + 16 * jt + 4 * fq) = pack4bf(acc); } }
.LBB0_934:
	ds_read_b32 v41, v108
	ds_read_b128 v[164:167], v88 offset:45056
	ds_read_b128 v[168:171], v88 offset:45120
	ds_read_b128 v[172:175], v88 offset:45184
	ds_read_b128 v[176:179], v88 offset:45248
	ds_read_b128 v[180:183], v115 offset:62464
	ds_read_b128 v[184:187], v115 offset:62528
	ds_read_b128 v[188:191], v115 offset:62592
	ds_read_b128 v[192:195], v115 offset:62656
	ds_read_b128 v[72:75], v89
	s_mov_b32 s0, 0x5040100
	v_mov_b32_e32 v152, 0
	v_mov_b32_e32 v153, 0
	v_mov_b32_e32 v154, 0
	v_mov_b32_e32 v155, 0
	v_mov_b32_e32 v156, 0
	v_mov_b32_e32 v157, 0
	v_mov_b32_e32 v158, 0
	v_mov_b32_e32 v159, 0
	v_mov_b32_e32 v148, 0
	v_mov_b32_e32 v149, 0
	v_mov_b32_e32 v150, 0
	v_mov_b32_e32 v151, 0
	s_and_b64 vcc, exec, s[44:45]
	s_cbranch_vccz .Lml_b_w0
	ds_read_b128 v[196:199], v116 offset:4352
	ds_read_b128 v[200:203], v116 offset:4416
	ds_read_b128 v[204:207], v116 offset:4480
	ds_read_b128 v[208:211], v116 offset:4544
	ds_read_b128 v[136:139], v89 offset:64
	s_andn2_b64 vcc, exec, s[46:47]
	s_cbranch_vccnz .Lml_b_w1
	ds_read_b128 v[212:215], v116 offset:8704
	ds_read_b128 v[216:219], v116 offset:8768
	ds_read_b128 v[220:223], v116 offset:8832
	ds_read_b128 v[224:227], v116 offset:8896
	ds_read_b128 v[140:143], v89 offset:128
	s_andn2_b64 vcc, exec, s[48:49]
	s_cbranch_vccnz .Lml_b_w2
	ds_read_b128 v[228:231], v116 offset:13056
	ds_read_b128 v[232:235], v116 offset:13120
	ds_read_b128 v[128:131], v116 offset:13184
	ds_read_b128 v[132:135], v116 offset:13248
	ds_read_b128 v[144:147], v89 offset:192
	s_waitcnt lgkmcnt(14)
	v_mfma_f32_16x16x32_bf16 v[68:71], v[180:183], v[164:167], 0
	v_mfma_f32_16x16x32_bf16 v[68:71], v[184:187], v[168:171], v[68:71]
	v_mfma_f32_16x16x32_bf16 v[68:71], v[188:191], v[172:175], v[68:71]
	v_mfma_f32_16x16x32_bf16 v[68:71], v[192:195], v[176:179], v[68:71]
	s_waitcnt lgkmcnt(10)
	v_mfma_f32_16x16x32_bf16 v[152:155], v[196:199], v[164:167], 0
	v_mfma_f32_16x16x32_bf16 v[152:155], v[200:203], v[168:171], v[152:155]
	v_mfma_f32_16x16x32_bf16 v[152:155], v[204:207], v[172:175], v[152:155]
	v_mfma_f32_16x16x32_bf16 v[152:155], v[208:211], v[176:179], v[152:155]
	s_waitcnt lgkmcnt(5)
	v_mfma_f32_16x16x32_bf16 v[156:159], v[212:215], v[164:167], 0
	v_mfma_f32_16x16x32_bf16 v[156:159], v[216:219], v[168:171], v[156:159]
	v_mfma_f32_16x16x32_bf16 v[156:159], v[220:223], v[172:175], v[156:159]
	v_mfma_f32_16x16x32_bf16 v[156:159], v[224:227], v[176:179], v[156:159]
	s_waitcnt lgkmcnt(0)
	v_mfma_f32_16x16x32_bf16 v[148:151], v[228:231], v[164:167], 0
	v_mfma_f32_16x16x32_bf16 v[148:151], v[232:235], v[168:171], v[148:151]
	v_mfma_f32_16x16x32_bf16 v[148:151], v[128:131], v[172:175], v[148:151]
	v_mfma_f32_16x16x32_bf16 v[148:151], v[132:135], v[176:179], v[148:151]
	s_branch .Lml_b_mm_done
.Lml_b_w2:
	s_waitcnt lgkmcnt(10)
	v_mfma_f32_16x16x32_bf16 v[68:71], v[180:183], v[164:167], 0
	v_mfma_f32_16x16x32_bf16 v[68:71], v[184:187], v[168:171], v[68:71]
	v_mfma_f32_16x16x32_bf16 v[68:71], v[188:191], v[172:175], v[68:71]
	v_mfma_f32_16x16x32_bf16 v[68:71], v[192:195], v[176:179], v[68:71]
	s_waitcnt lgkmcnt(5)
	v_mfma_f32_16x16x32_bf16 v[152:155], v[196:199], v[164:167], 0
	v_mfma_f32_16x16x32_bf16 v[152:155], v[200:203], v[168:171], v[152:155]
	v_mfma_f32_16x16x32_bf16 v[152:155], v[204:207], v[172:175], v[152:155]
	v_mfma_f32_16x16x32_bf16 v[152:155], v[208:211], v[176:179], v[152:155]
	s_waitcnt lgkmcnt(0)
	v_mfma_f32_16x16x32_bf16 v[156:159], v[212:215], v[164:167], 0
	v_mfma_f32_16x16x32_bf16 v[156:159], v[216:219], v[168:171], v[156:159]
	v_mfma_f32_16x16x32_bf16 v[156:159], v[220:223], v[172:175], v[156:159]
	v_mfma_f32_16x16x32_bf16 v[156:159], v[224:227], v[176:179], v[156:159]
	s_branch .Lml_b_mm_done
.Lml_b_w1:
	s_waitcnt lgkmcnt(5)
	v_mfma_f32_16x16x32_bf16 v[68:71], v[180:183], v[164:167], 0
	v_mfma_f32_16x16x32_bf16 v[68:71], v[184:187], v[168:171], v[68:71]
	v_mfma_f32_16x16x32_bf16 v[68:71], v[188:191], v[172:175], v[68:71]
	v_mfma_f32_16x16x32_bf16 v[68:71], v[192:195], v[176:179], v[68:71]
	s_waitcnt lgkmcnt(0)
	v_mfma_f32_16x16x32_bf16 v[152:155], v[196:199], v[164:167], 0
	v_mfma_f32_16x16x32_bf16 v[152:155], v[200:203], v[168:171], v[152:155]
	v_mfma_f32_16x16x32_bf16 v[152:155], v[204:207], v[172:175], v[152:155]
	v_mfma_f32_16x16x32_bf16 v[152:155], v[208:211], v[176:179], v[152:155]
	s_branch .Lml_b_mm_done
.Lml_b_w0:
	s_waitcnt lgkmcnt(0)
	v_mfma_f32_16x16x32_bf16 v[68:71], v[180:183], v[164:167], 0
	v_mfma_f32_16x16x32_bf16 v[68:71], v[184:187], v[168:171], v[68:71]
	v_mfma_f32_16x16x32_bf16 v[68:71], v[188:191], v[172:175], v[68:71]
	v_mfma_f32_16x16x32_bf16 v[68:71], v[192:195], v[176:179], v[68:71]
.Lml_b_mm_done:
	s_nop 7
	v_sub_f32_e32 v67, v72, v41
	v_mul_f32_e32 v67, 0x3fb8aa3b, v67
	v_exp_f32_e32 v67, v67
	s_nop 2
	v_mul_f32_e32 v67, v68, v67
	v_sub_f32_e32 v68, v73, v41
	v_mul_f32_e32 v68, 0x3fb8aa3b, v68
	v_exp_f32_e32 v68, v68
	v_cndmask_b32_e64 v67, v67, 0, s[6:7]
	v_mul_f32_e32 v68, v69, v68
	v_cndmask_b32_e64 v72, 0, v68, s[8:9]
	v_sub_f32_e32 v68, v74, v41
	v_sub_f32_e32 v69, v75, v41
	v_mul_f32_e32 v68, 0x3fb8aa3b, v68
	v_mul_f32_e32 v69, 0x3fb8aa3b, v69
	v_exp_f32_e32 v68, v68
	v_exp_f32_e32 v69, v69
	s_nop 0
	v_pk_mul_f32 v[68:69], v[70:71], v[68:69]
	v_cvt_pk_bf16_f32 v70, v67, v72
	v_cvt_pk_bf16_f32 v67, v68, v69
	v_cndmask_b32_e64 v68, v67, 0, s[12:13]
	v_lshrrev_b32_e32 v67, 16, v67
	v_cndmask_b32_e64 v67, v67, 0, s[10:11]
	v_perm_b32 v71, v67, v68, s0
	ds_write_b64 v110, v[70:71]
	v_mov_b32_e32 v67, 0
	s_and_b64 vcc, exec, s[44:45]
	s_cbranch_vccz .Lml_b_tail1
	v_sub_f32_e32 v136, v136, v41
	v_sub_f32_e32 v137, v137, v41
	v_sub_f32_e32 v138, v138, v41
	v_sub_f32_e32 v139, v139, v41
	v_mul_f32_e32 v136, 0x3fb8aa3b, v136
	v_mul_f32_e32 v137, 0x3fb8aa3b, v137
	v_mul_f32_e32 v138, 0x3fb8aa3b, v138
	v_mul_f32_e32 v139, 0x3fb8aa3b, v139
	v_exp_f32_e32 v136, v136
	v_exp_f32_e32 v137, v137
	v_exp_f32_e32 v138, v138
	v_exp_f32_e32 v139, v139
	v_pk_mul_f32 v[152:153], v[152:153], v[136:137]
	s_nop 0
	v_cndmask_b32_e64 v152, v152, 0, s[20:21]
	v_pk_mul_f32 v[154:155], v[154:155], v[138:139]
	v_cndmask_b32_e64 v153, v153, 0, s[18:19]
	v_cndmask_b32_e64 v154, v154, 0, s[16:17]
	v_cndmask_b32_e64 v155, v155, 0, s[14:15]
